# background conversion in NSA tile loop v2 (lean block, counted waits, foreground slot 15 moved, no drain before chunk routine)
# baseline (speedup 1.0000x reference)
.LBB0_2337:
	s_mov_b32 s32, 0
	s_nop 0
	s_nop 0
	s_nop 0
	s_nop 0
	s_nop 0
	s_nop 0
	s_nop 0
	s_nop 0
	s_nop 0
	s_nop 0
	s_nop 0
	s_nop 0
	s_nop 0
	s_nop 0
	s_nop 0
	v_mov_b32_e32 v91, v0
	s_nop 0
	v_readfirstlane_b32 s95, v91
	s_ashr_i32 s75, s95, 6
	s_cmp_lt_i32 s75, 4
	s_cbranch_scc1 .LBB0_2339
	s_setprio 1

.LBB0_2419:
	s_lshl_b32 s2, s2, 13
	s_add_i32 s76, s2, 0
	s_add_i32 s76, s76, 0x10000
	s_andn2_b64 vcc, exec, s[8:9]
	v_lshlrev_b32_e32 v134, 2, v162
	s_cbranch_vccnz .LBB0_2468
	v_or_b32_e32 v6, 32, v168
	v_cmp_gt_i32_e64 s[40:41], v6, v2
	v_cmp_lt_i32_e64 s[42:43], v6, v2
	v_or_b32_e32 v6, 34, v168
	v_cmp_gt_i32_e64 s[44:45], v6, v2
	v_or_b32_e32 v6, 35, v168
	v_cmp_gt_i32_e64 s[46:47], v6, v2
	v_or_b32_e32 v6, 40, v168
	v_cmp_gt_i32_e64 s[48:49], v6, v2
	v_or_b32_e32 v6, 41, v168
	v_cmp_gt_i32_e64 s[50:51], v6, v2
	v_or_b32_e32 v6, 42, v168
	v_cmp_gt_i32_e64 s[52:53], v6, v2
	v_or_b32_e32 v6, 43, v168
	v_cmp_gt_i32_e64 s[54:55], v6, v2
	v_or_b32_e32 v6, 48, v168
	v_cmp_gt_i32_e64 s[56:57], v6, v2
	v_or_b32_e32 v6, 49, v168
	v_cmp_gt_i32_e64 s[58:59], v6, v2
	v_or_b32_e32 v6, 50, v168
	v_cmp_gt_i32_e64 s[60:61], v6, v2
	v_or_b32_e32 v6, 51, v168
	v_cmp_gt_i32_e64 s[62:63], v6, v2
	v_or_b32_e32 v6, 56, v168
	v_cmp_gt_i32_e64 s[64:65], v6, v2
	v_or_b32_e32 v6, 57, v168
	v_cmp_gt_i32_e64 s[66:67], v6, v2
	v_or_b32_e32 v6, 58, v168
	v_cmp_gt_i32_e64 s[68:69], v6, v2
	v_or_b32_e32 v6, 59, v168
	v_cmp_gt_i32_e64 s[6:7], v168, v2
	v_cmp_lt_i32_e64 s[8:9], v168, v2
	v_cmp_gt_i32_e64 s[10:11], v135, v2
	v_cmp_gt_i32_e64 s[12:13], v169, v2
	v_cmp_gt_i32_e64 s[14:15], v170, v2
	v_cmp_gt_i32_e64 s[16:17], v171, v2
	v_cmp_gt_i32_e64 s[18:19], v172, v2
	v_cmp_gt_i32_e64 s[20:21], v173, v2
	v_cmp_gt_i32_e64 s[22:23], v174, v2
	v_cmp_gt_i32_e64 s[24:25], v175, v2
	v_cmp_gt_i32_e64 s[26:27], v176, v2
	v_cmp_gt_i32_e64 s[28:29], v177, v2
	v_cmp_gt_i32_e64 s[30:31], v178, v2
	v_cmp_gt_i32_e64 s[34:35], v179, v2
	v_cmp_gt_i32_e64 s[36:37], v180, v2
	v_cmp_gt_i32_e64 s[38:39], v181, v2
	v_cmp_gt_i32_e64 s[70:71], v6, v2
	s_min_u32 s2, s92, 8
	v_lshlrev_b32_e32 v2, 4, v4
	s_add_i32 s2, s92, s2
	v_and_b32_e32 v2, 0xc0, v2
	s_lshl_b32 s87, s2, 13
	v_lshl_or_b32 v2, v160, 8, v2
	v_readlane_b32 s2, v247, 4
	v_lshlrev_b32_e32 v5, 1, v4
	v_mov_b32_e32 v140, 0
	v_add_u32_e32 v185, s2, v2
	v_readlane_b32 s2, v247, 5
	s_movk_i32 s96, 0xc00
	s_add_i32 s91, s91, s92
	v_add_u32_e32 v187, s2, v2
	v_readlane_b32 s2, v247, 6
	s_add_i32 s93, s93, s3
	v_mov_b32_e32 v139, v131
	v_add_u32_e32 v188, s2, v2
	v_readlane_b32 s2, v247, 7
	s_mov_b32 s94, 2
	v_add_u32_e32 v183, s75, v134
	v_add_u32_e32 v189, s2, v2
	v_readlane_b32 s2, v247, 8
	v_add3_u32 v184, s76, v166, v134
	s_lshl_b32 s95, s92, 13
	v_add_u32_e32 v190, s2, v2
	v_readlane_b32 s2, v247, 9
	s_addk_i32 s87, 0x4000
	v_and_or_b32 v186, v5, 32, v3
	v_add_u32_e32 v191, s2, v2
	v_readlane_b32 s2, v247, 10
	s_add_i32 s86, s75, 0xc000
	s_mov_b32 s3, 0
	v_add_u32_e32 v192, s2, v2
	v_readlane_b32 s2, v247, 11
	v_mov_b32_e32 v202, 0
	v_mov_b32_e32 v3, v140
	v_add_u32_e32 v193, s2, v2
	v_readlane_b32 s2, v247, 12
	v_mov_b32_e32 v4, v140
	v_mov_b32_e32 v5, v140
	v_add_u32_e32 v194, s2, v2
	v_readlane_b32 s2, v247, 13
	v_mov_b32_e32 v6, v140
	v_mov_b32_e32 v7, v140
	v_add_u32_e32 v195, s2, v2
	v_readlane_b32 s2, v247, 14
	v_mov_b32_e32 v8, v140
	v_mov_b32_e32 v9, v140
	v_add_u32_e32 v196, s2, v2
	v_readlane_b32 s2, v247, 15
	v_mov_b32_e32 v10, v140
	v_mov_b32_e32 v11, v140
	v_add_u32_e32 v197, s2, v2
	v_readlane_b32 s2, v247, 16
	v_mov_b32_e32 v12, v140
	v_mov_b32_e32 v13, v140
	v_add_u32_e32 v198, s2, v2
	v_readlane_b32 s2, v247, 17
	v_mov_b32_e32 v14, v140
	v_mov_b32_e32 v15, v140
	v_add_u32_e32 v199, s2, v2
	v_readlane_b32 s2, v247, 21
	v_mov_b32_e32 v16, v140
	v_mov_b32_e32 v17, v140
	v_add_u32_e32 v200, s2, v2
	s_add_i32 s2, 0, 0x8000
	v_add_u32_e32 v201, s2, v2
	s_mov_b32 s2, 0
	v_mov_b32_e32 v2, 0
	v_mov_b32_e32 v18, 0
	v_mov_b32_e32 v19, v140
	v_mov_b32_e32 v20, v140
	v_mov_b32_e32 v21, v140
	v_mov_b32_e32 v22, v140
	v_mov_b32_e32 v23, v140
	v_add_u32_e32 v226, v201, v186
	v_mov_b32_e32 v24, v140
	v_mov_b32_e32 v25, v140
	v_mov_b32_e32 v26, v140
	v_mov_b32_e32 v27, v140
	v_mov_b32_e32 v28, v140
	v_mov_b32_e32 v29, v140
	v_mov_b32_e32 v30, v140
	v_mov_b32_e32 v31, v140
	v_mov_b32_e32 v32, v140
	v_mov_b32_e32 v33, v140
	s_mov_b32 s32, 0
	v_readlane_b32 s72, v249, 50
	s_cmp_gt_i32 s72, 7
	s_cbranch_scc1 .LBB0_2422
	s_mul_i32 s72, s72, 48
	v_readlane_b32 s73, v248, 47
	s_add_i32 s72, s73, s72
	v_readlane_b32 s78, v248, 48
	s_add_i32 s73, s72, 48
	s_min_i32 s78, s78, s73
	s_min_i32 s78, s78, 0x1be90
	v_readlane_b32 s84, v249, 16
	s_add_i32 s73, s72, s84
	s_cmp_ge_i32 s73, s78
	s_cbranch_scc1 .LBB0_2422
	v_writelane_b32 v244, s78, 3
	s_lshl_b32 s84, s84, 11
	s_add_i32 s84, s84, 0x24000
	v_and_b32_e32 v50, 63, v0
	v_and_b32_e32 v51, 31, v50
	v_lshrrev_b32_e32 v52, 5, v50
	v_lshlrev_b32_e32 v52, 10, v52
	v_lshl_add_u32 v51, v51, 2, v52
	v_add_u32_e32 v245, s84, v51
	s_mov_b32 s85, 2
	s_mov_b32 s32, 0x30
	s_branch .Lbgn_dec
.Lbgn_new:
	v_readlane_b32 s73, v244, 4
	v_readlane_b32 s78, v244, 3
	s_and_b32 s85, s32, 1
	s_add_i32 s73, s73, 8
	s_cmp_ge_i32 s73, s78
	s_cbranch_scc0 .Lbgn_dec
	s_andn2_b32 s32, s32, 0x50
	s_branch .Lbgn_end
.Lbgn_dec:
	v_writelane_b32 v244, s73, 4
	v_readlane_b32 s82, v249, 1
	v_readlane_b32 s83, v249, 2
	s_sub_u32 s72, s73, 0x3e90
	s_lshr_b32 vcc_lo, s72, 15
	s_and_b32 s72, s72, 0x7fff
	s_lshl_b32 vcc_hi, vcc_lo, 3
	s_addk_i32 vcc_hi, 0xa8
	s_load_dwordx2 s[98:99], s[82:83], vcc_hi
	s_load_dwordx2 s[78:79], s[82:83], 0xe0
	s_lshr_b32 vcc_hi, s72, 9
	s_and_b32 s72, s72, 0x1ff
	s_cmp_eq_u32 vcc_lo, 2
	s_cbranch_scc1 .Lbgn_dn
	s_lshr_b32 s73, s72, 4
	s_and_b32 s72, s72, 15
	s_lshl_b32 s100, vcc_hi, 21
	s_lshl_b32 s101, vcc_hi, 22
	s_lshl_b32 vcc_hi, s73, 6
	s_add_u32 s100, s100, vcc_hi
	s_lshl_b32 vcc_hi, s73, 17
	s_add_u32 s101, s101, vcc_hi
	s_lshl_b32 vcc_hi, s72, 7
	s_add_u32 s101, s101, vcc_hi
	s_lshr_b32 vcc_hi, s72, 2
	s_lshl_b32 vcc_hi, vcc_hi, 19
	s_add_u32 s100, s100, vcc_hi
	s_and_b32 vcc_hi, s72, 3
	s_lshl_b32 vcc_hi, vcc_hi, 16
	s_add_u32 s100, s100, vcc_hi
	s_lshl_b32 vcc_hi, vcc_lo, 18
	s_add_u32 s100, s100, vcc_hi
	s_add_u32 s100, s100, 0x1b000000
	s_bitset0_b32 s32, 0
	s_branch .Lbgn_dd
.Lbgn_dn:
	s_lshr_b32 s73, s72, 6
	s_and_b32 s72, s72, 63
	s_lshl_b32 s100, vcc_hi, 20
	s_lshl_b32 s101, vcc_hi, 22
	s_lshl_b32 vcc_hi, s73, 6
	s_add_u32 s100, s100, vcc_hi
	s_lshl_b32 vcc_hi, s73, 19
	s_add_u32 s101, s101, vcc_hi
	s_lshl_b32 vcc_hi, s72, 7
	s_add_u32 s101, s101, vcc_hi
	s_lshl_b32 vcc_hi, s72, 14
	s_add_u32 s100, s100, vcc_hi
	s_add_u32 s100, s100, 0x2000000
	s_bitset1_b32 s32, 0
.Lbgn_dd:
	s_waitcnt lgkmcnt(0)
	s_add_u32 s98, s98, s101
	s_addc_u32 s99, s99, 0
	s_add_u32 s100, s78, s100
	s_addc_u32 s101, s79, 0
	s_and_b32 s72, s32, 1
	s_cmp_eq_u32 s72, s85
	s_cbranch_scc1 .Lbgn_same
	s_cmp_eq_u32 s72, 1
	s_cselect_b32 s97, 13, 11
	s_cselect_b32 s85, 9, 11
	s_mov_b32 s72, 0x8000
	s_cselect_b32 s72, 0x20000, s72
	v_and_b32_e32 v50, 63, v0
	v_lshrrev_b32_e32 v51, 3, v50
	v_and_b32_e32 v52, 7, v50
	v_lshlrev_b32_e32 v51, s97, v51
	v_lshl_add_u32 v51, v52, 4, v51
	v_and_b32_e32 v53, 31, v50
	v_lshrrev_b32_e32 v52, 5, v50
	v_lshlrev_b32_e32 v53, s85, v53
	v_lshl_add_u32 v53, v52, 3, v53
	v_lshl_or_b32 v246, v53, 16, v51
	v_writelane_b32 v244, s72, 5
	v_and_b32_e32 v52, 0xffff, v246
.Lbgn_same:
	v_readlane_b32 s72, v244, 5
	s_bitcmp1_b32 s32, 5
	s_cbranch_scc0 .Lbgn_issue
	s_mov_b32 m0, s84
	s_andn2_b32 s32, s32, 0x20
	global_load_lds_dwordx4 v52, s[98:99] nt
	s_branch .Lbgn_issue
	s_nop 0
	s_nop 0
	s_nop 0
	s_nop 0
	s_nop 0
	s_nop 0
	s_nop 0
	s_nop 0
	s_nop 0
	s_nop 0
	s_nop 0
	s_nop 0
	s_nop 0
	s_nop 0
	s_branch .LBB0_2422

.LBB0_2422:
	s_bitcmp1_b32 s32, 4
	s_cbranch_scc0 .Lbgn_end
	s_add_i32 s80, s3, 2
	s_cmp_lt_u32 s80, s90
	s_cbranch_scc1 .Lbgn_w2
	s_cmp_lt_u32 s3, s91
	s_cbranch_scc1 .Lbgn_w1
	s_waitcnt vmcnt(0)
	s_branch .Lbgn_wd
.Lbgn_w1:
	s_waitcnt vmcnt(1)
	s_branch .Lbgn_wd

.Lbgn_wd:
	ds_read2_b32 v[54:55], v245 offset1:32
	ds_read2_b32 v[56:57], v245 offset0:64 offset1:96
	ds_read2_b32 v[58:59], v245 offset0:128 offset1:160
	ds_read2_b32 v[60:61], v245 offset0:192 offset1:224
	v_lshrrev_b32_e32 v53, 16, v246
	v_and_b32_e32 v52, 0xffff, v246
	v_mov_b32_e32 v62, 0x42800000
	v_readlane_b32 s72, v244, 5
	v_readfirstlane_b32 s84, v245
	s_waitcnt lgkmcnt(0)
	v_pk_mul_f32 v[54:55], v[54:55], v[62:63] op_sel_hi:[1,0]
	v_pk_mul_f32 v[56:57], v[56:57], v[62:63] op_sel_hi:[1,0]
	v_pk_mul_f32 v[58:59], v[58:59], v[62:63] op_sel_hi:[1,0]
	v_pk_mul_f32 v[60:61], v[60:61], v[62:63] op_sel_hi:[1,0]
	v_cvt_pk_fp8_f32 v64, v54, v55
	v_cvt_pk_fp8_f32 v65, v58, v59
	v_cvt_pk_fp8_f32 v64, v56, v57 op_sel:[0,0,1]
	v_cvt_pk_fp8_f32 v65, v60, v61 op_sel:[0,0,1]
	s_addk_i32 s32, 0x100
	global_store_dwordx2 v53, v[64:65], s[100:101]
	s_add_u32 s100, s100, 16
	s_and_b32 s73, s100, 0x30
	s_cbranch_scc0 .Lbgn_new
	s_add_u32 s98, s98, s72
	s_addc_u32 s99, s99, 0
.Lbgn_issue:
	s_mov_b32 m0, s84
	s_lshr_b32 s72, s72, 1
	s_add_u32 s80, s98, s72
	s_addc_u32 s81, s99, 0
	global_load_lds_dwordx4 v52, s[98:99] nt
	s_add_i32 m0, m0, 0x400
	s_nop 0
	global_load_lds_dwordx4 v52, s[80:81] nt
.Lbgn_end:
	s_mul_hi_u32 s97, s3, 0xaaaaaaab
	s_lshr_b32 s97, s97, 1
	s_mulk_i32 s97, 0xa000
	s_add_i32 s97, s97, s2
	v_add_u32_e32 v225, s97, v226
	s_add_i32 s80, s3, 2
	s_cmp_lt_u32 s80, s90
	s_cselect_b64 s[72:73], -1, 0
	s_cmp_ge_u32 s80, s90
	s_mov_b64 s[78:79], -1
	s_cbranch_scc0 .LBB0_2430
	s_cmp_ge_u32 s3, s91
	s_cbranch_scc0 .LBB0_2425
	s_bitcmp1_b32 s32, 4
	s_cbranch_scc1 .Lbgn_h0a
	s_waitcnt vmcnt(0) lgkmcnt(0)
	s_branch .Lbgn_h0b

.LBB0_2425:
	s_andn2_b64 vcc, exec, s[78:79]
	s_cbranch_vccnz .LBB0_2427
	s_bitcmp1_b32 s32, 4
	s_cbranch_scc1 .Lbgn_h1a
	s_waitcnt vmcnt(1) lgkmcnt(0)
	s_branch .Lbgn_h1b

.LBB0_2431:
	s_bitcmp1_b32 s32, 4
	s_cbranch_scc1 .Lbgn_h2a
	s_waitcnt vmcnt(2) lgkmcnt(0)
	s_branch .Lbgn_h2b
	s_nop 0
	s_nop 0
	s_nop 0
	s_nop 0

.LBB0_2471:
	s_or_b64 exec, exec, s[6:7]
	s_waitcnt lgkmcnt(0)
	v_lshl_add_u32 v51, v160, 4, s75
	v_add3_u32 v50, s76, v166, v134
	ds_read_b32 v54, v51 offset:57472
	ds_read2_b32 v[52:53], v50 offset1:32
	s_lshl_b32 s2, s2, 1
	v_readlane_b32 s3, v249, 61
	s_add_u32 s2, s3, s2
	v_readlane_b32 s3, v249, 36
	s_waitcnt lgkmcnt(0)
	v_fma_f32 v2, v2, v54, v52
	v_fmac_f32_e32 v53, v18, v54
	ds_write2_b32 v50, v2, v53 offset1:32
	ds_read_b32 v2, v51 offset:57476
	ds_read2_b32 v[52:53], v50 offset0:64 offset1:96
	s_addc_u32 s3, s3, 0
	s_waitcnt lgkmcnt(0)
	v_fma_f32 v3, v3, v2, v52
	v_fmac_f32_e32 v53, v19, v2
	ds_write2_b32 v50, v3, v53 offset0:64 offset1:96
	ds_read_b32 v18, v51 offset:57480
	ds_read2_b32 v[2:3], v50 offset0:128 offset1:160
	v_add_u32_e32 v19, 0x1000, v50
	s_waitcnt lgkmcnt(0)
	v_fma_f32 v2, v4, v18, v2
	v_fmac_f32_e32 v3, v20, v18
	ds_write2_b32 v50, v2, v3 offset0:128 offset1:160
	ds_read_b32 v4, v51 offset:57484
	ds_read2_b32 v[2:3], v50 offset0:192 offset1:224
	v_add_u32_e32 v18, 0x800, v50
	v_add_u32_e32 v20, 0x1800, v50
	s_waitcnt lgkmcnt(0)
	v_fma_f32 v2, v5, v4, v2
	v_fmac_f32_e32 v3, v21, v4
	ds_write2_b32 v50, v2, v3 offset0:192 offset1:224
	ds_read_b32 v4, v51 offset:57504
	ds_read2_b32 v[2:3], v18 offset1:32
	s_waitcnt lgkmcnt(0)
	v_fma_f32 v2, v6, v4, v2
	v_fmac_f32_e32 v3, v22, v4
	ds_write2_b32 v18, v2, v3 offset1:32
	ds_read_b32 v4, v51 offset:57508
	ds_read2_b32 v[2:3], v18 offset0:64 offset1:96
	s_waitcnt lgkmcnt(0)
	v_fma_f32 v2, v7, v4, v2
	v_fmac_f32_e32 v3, v23, v4
	ds_write2_b32 v18, v2, v3 offset0:64 offset1:96
	ds_read_b32 v4, v51 offset:57512
	ds_read2_b32 v[2:3], v18 offset0:128 offset1:160
	s_waitcnt lgkmcnt(0)
	v_fma_f32 v2, v8, v4, v2
	v_fmac_f32_e32 v3, v24, v4
	ds_write2_b32 v18, v2, v3 offset0:128 offset1:160
	ds_read_b32 v4, v51 offset:57516
	ds_read2_b32 v[2:3], v18 offset0:192 offset1:224
	s_waitcnt lgkmcnt(0)
	v_fma_f32 v2, v9, v4, v2
	v_fmac_f32_e32 v3, v25, v4
	ds_write2_b32 v18, v2, v3 offset0:192 offset1:224
	ds_read_b32 v4, v51 offset:57536
	ds_read2_b32 v[2:3], v19 offset1:32
	s_waitcnt lgkmcnt(0)
	v_fma_f32 v2, v10, v4, v2
	v_fmac_f32_e32 v3, v26, v4
	ds_write2_b32 v19, v2, v3 offset1:32
	ds_read_b32 v4, v51 offset:57540
	ds_read2_b32 v[2:3], v19 offset0:64 offset1:96
	s_waitcnt lgkmcnt(0)
	v_fma_f32 v2, v11, v4, v2
	v_fmac_f32_e32 v3, v27, v4
	ds_write2_b32 v19, v2, v3 offset0:64 offset1:96
	ds_read_b32 v4, v51 offset:57544
	ds_read2_b32 v[2:3], v19 offset0:128 offset1:160
	s_waitcnt lgkmcnt(0)
	v_fma_f32 v2, v12, v4, v2
	v_fmac_f32_e32 v3, v28, v4
	ds_write2_b32 v19, v2, v3 offset0:128 offset1:160
	ds_read_b32 v4, v51 offset:57548
	ds_read2_b32 v[2:3], v19 offset0:192 offset1:224
	s_waitcnt lgkmcnt(0)
	v_fma_f32 v2, v13, v4, v2
	v_fmac_f32_e32 v3, v29, v4
	ds_write2_b32 v19, v2, v3 offset0:192 offset1:224
	ds_read_b32 v4, v51 offset:57568
	ds_read2_b32 v[2:3], v20 offset1:32
	s_waitcnt lgkmcnt(0)
	v_fma_f32 v2, v14, v4, v2
	v_fmac_f32_e32 v3, v30, v4
	ds_write2_b32 v20, v2, v3 offset1:32
	ds_read_b32 v4, v51 offset:57572
	ds_read2_b32 v[2:3], v20 offset0:64 offset1:96
	s_waitcnt lgkmcnt(0)
	v_fma_f32 v2, v15, v4, v2
	v_fmac_f32_e32 v3, v31, v4
	ds_write2_b32 v20, v2, v3 offset0:64 offset1:96
	ds_read_b32 v4, v51 offset:57576
	ds_read2_b32 v[2:3], v20 offset0:128 offset1:160
	s_waitcnt lgkmcnt(0)
	v_fma_f32 v2, v16, v4, v2
	v_fmac_f32_e32 v3, v32, v4
	ds_write2_b32 v20, v2, v3 offset0:128 offset1:160
	ds_read_b32 v4, v51 offset:57580
	ds_read2_b32 v[2:3], v20 offset0:192 offset1:224
	s_waitcnt lgkmcnt(0)
	v_fma_f32 v2, v17, v4, v2
	v_fmac_f32_e32 v3, v33, v4
	ds_write2_b32 v20, v2, v3 offset0:192 offset1:224
	v_mov_b64_e32 v[2:3], v[66:67]
	s_waitcnt lgkmcnt(0)
	v_mov_b64_e32 v[4:5], v[68:69]
	v_mov_b64_e32 v[6:7], v[70:71]
	v_mov_b64_e32 v[8:9], v[72:73]
	v_mov_b64_e32 v[10:11], v[74:75]
	v_mov_b64_e32 v[12:13], v[76:77]
	v_mov_b64_e32 v[14:15], v[78:79]
	v_mov_b64_e32 v[16:17], v[80:81]
	ds_read2_b32 v[2:3], v50 offset1:32
	s_waitcnt vmcnt(31) lgkmcnt(0)
	v_add_f32_e32 v4, v96, v2
	s_waitcnt vmcnt(30)
	v_add_f32_e32 v5, v97, v3
	ds_read2_b32 v[2:3], v50 offset0:64 offset1:96
	s_waitcnt vmcnt(29) lgkmcnt(0)
	v_add_f32_e32 v6, v94, v2
	s_waitcnt vmcnt(28)
	v_add_f32_e32 v7, v95, v3
	ds_read2_b32 v[2:3], v50 offset0:128 offset1:160
	s_waitcnt vmcnt(27) lgkmcnt(0)
	v_add_f32_e32 v8, v92, v2
	s_waitcnt vmcnt(26)
	v_add_f32_e32 v9, v93, v3
	ds_read2_b32 v[2:3], v50 offset0:192 offset1:224
	s_waitcnt vmcnt(25) lgkmcnt(0)
	v_add_f32_e32 v10, v90, v2
	s_waitcnt vmcnt(24)
	v_add_f32_e32 v11, v91, v3
	ds_read2_b32 v[2:3], v18 offset1:32
	s_waitcnt vmcnt(23) lgkmcnt(0)
	v_add_f32_e32 v12, v86, v2
	s_waitcnt vmcnt(22)
	v_add_f32_e32 v13, v87, v3
	ds_read2_b32 v[2:3], v18 offset0:64 offset1:96
	s_waitcnt vmcnt(21) lgkmcnt(0)
	v_add_f32_e32 v14, v84, v2
	s_waitcnt vmcnt(20)
	v_add_f32_e32 v15, v85, v3
	ds_read2_b32 v[2:3], v18 offset0:128 offset1:160
	s_waitcnt vmcnt(19) lgkmcnt(0)
	v_add_f32_e32 v16, v82, v2
	s_waitcnt vmcnt(18)
	v_add_f32_e32 v17, v83, v3
	ds_read2_b32 v[2:3], v18 offset0:192 offset1:224
	s_waitcnt vmcnt(17) lgkmcnt(0)
	v_add_f32_e32 v18, v46, v2
	s_waitcnt vmcnt(16)
	v_add_f32_e32 v21, v47, v3
	ds_read2_b32 v[2:3], v19 offset1:32
	s_waitcnt vmcnt(15) lgkmcnt(0)
	v_add_f32_e32 v22, v58, v2
	s_waitcnt vmcnt(14)
	v_add_f32_e32 v23, v59, v3
	ds_read2_b32 v[2:3], v19 offset0:64 offset1:96
	s_waitcnt vmcnt(13) lgkmcnt(0)
	v_add_f32_e32 v24, v48, v2
	s_waitcnt vmcnt(12)
	v_add_f32_e32 v25, v49, v3
	ds_read2_b32 v[2:3], v19 offset0:128 offset1:160
	s_waitcnt vmcnt(11) lgkmcnt(0)
	v_add_f32_e32 v26, v44, v2
	s_waitcnt vmcnt(10)
	v_add_f32_e32 v27, v45, v3
	ds_read2_b32 v[2:3], v19 offset0:192 offset1:224
	s_waitcnt vmcnt(9) lgkmcnt(0)
	v_add_f32_e32 v19, v40, v2
	s_waitcnt vmcnt(8)
	v_add_f32_e32 v28, v41, v3
	ds_read2_b32 v[2:3], v20 offset1:32
	s_waitcnt vmcnt(7) lgkmcnt(0)
	v_add_f32_e32 v29, v42, v2
	s_waitcnt vmcnt(6)
	v_add_f32_e32 v30, v43, v3
	ds_read2_b32 v[2:3], v20 offset0:64 offset1:96
	s_waitcnt vmcnt(5) lgkmcnt(0)
	v_add_f32_e32 v31, v38, v2
	s_waitcnt vmcnt(4)
	v_add_f32_e32 v32, v39, v3
	ds_read2_b32 v[2:3], v20 offset0:128 offset1:160
	s_waitcnt vmcnt(3) lgkmcnt(0)
	v_add_f32_e32 v33, v36, v2
	s_waitcnt vmcnt(2)
	v_add_f32_e32 v36, v37, v3
	ds_read2_b32 v[2:3], v20 offset0:192 offset1:224
	v_lshlrev_b32_e32 v20, 9, v160
	s_waitcnt lgkmcnt(0)
	s_waitcnt vmcnt(1) lgkmcnt(0)
	v_add_f32_e32 v2, v34, v2
	v_lshlrev_b32_e32 v34, 1, v162
	v_add3_u32 v20, s76, v20, v34
	v_bfe_u32 v34, v4, 16, 1
	v_add3_u32 v4, v4, v34, s74
	ds_write_b16_d16_hi v20, v4
	v_bfe_u32 v4, v5, 16, 1
	v_add3_u32 v4, v5, v4, s74
	ds_write_b16_d16_hi v20, v4 offset:64
	v_bfe_u32 v4, v6, 16, 1
	v_add3_u32 v4, v6, v4, s74
	ds_write_b16_d16_hi v20, v4 offset:128
	v_bfe_u32 v4, v7, 16, 1
	v_add3_u32 v4, v7, v4, s74
	ds_write_b16_d16_hi v20, v4 offset:192
	v_bfe_u32 v4, v8, 16, 1
	v_add3_u32 v4, v8, v4, s74
	ds_write_b16_d16_hi v20, v4 offset:256
	v_bfe_u32 v4, v9, 16, 1
	v_add3_u32 v4, v9, v4, s74
	ds_write_b16_d16_hi v20, v4 offset:320
	v_bfe_u32 v4, v10, 16, 1
	v_add3_u32 v4, v10, v4, s74
	ds_write_b16_d16_hi v20, v4 offset:384
	v_bfe_u32 v4, v11, 16, 1
	v_add3_u32 v4, v11, v4, s74
	ds_write_b16_d16_hi v20, v4 offset:448
	v_bfe_u32 v4, v12, 16, 1
	v_add3_u32 v4, v12, v4, s74
	ds_write_b16_d16_hi v20, v4 offset:1024
	v_bfe_u32 v4, v13, 16, 1
	v_add3_u32 v4, v13, v4, s74
	ds_write_b16_d16_hi v20, v4 offset:1088
	v_bfe_u32 v4, v14, 16, 1
	v_add3_u32 v4, v14, v4, s74
	ds_write_b16_d16_hi v20, v4 offset:1152
	v_bfe_u32 v4, v15, 16, 1
	v_add3_u32 v4, v15, v4, s74
	ds_write_b16_d16_hi v20, v4 offset:1216
	v_bfe_u32 v4, v16, 16, 1
	v_add3_u32 v4, v16, v4, s74
	ds_write_b16_d16_hi v20, v4 offset:1280
	v_bfe_u32 v4, v17, 16, 1
	v_add3_u32 v4, v17, v4, s74
	ds_write_b16_d16_hi v20, v4 offset:1344
	v_bfe_u32 v4, v18, 16, 1
	v_add3_u32 v4, v18, v4, s74
	ds_write_b16_d16_hi v20, v4 offset:1408
	v_bfe_u32 v4, v21, 16, 1
	v_add3_u32 v4, v21, v4, s74
	ds_write_b16_d16_hi v20, v4 offset:1472
	v_bfe_u32 v4, v22, 16, 1
	v_add3_u32 v4, v22, v4, s74
	ds_write_b16_d16_hi v20, v4 offset:2048
	v_bfe_u32 v4, v23, 16, 1
	v_add3_u32 v4, v23, v4, s74
	ds_write_b16_d16_hi v20, v4 offset:2112
	v_bfe_u32 v4, v24, 16, 1
	v_add3_u32 v4, v24, v4, s74
	ds_write_b16_d16_hi v20, v4 offset:2176
	v_bfe_u32 v4, v25, 16, 1
	v_add3_u32 v4, v25, v4, s74
	ds_write_b16_d16_hi v20, v4 offset:2240
	v_bfe_u32 v4, v26, 16, 1
	v_add3_u32 v4, v26, v4, s74
	ds_write_b16_d16_hi v20, v4 offset:2304
	v_bfe_u32 v4, v27, 16, 1
	v_add3_u32 v4, v27, v4, s74
	ds_write_b16_d16_hi v20, v4 offset:2368
	v_bfe_u32 v4, v19, 16, 1
	v_add3_u32 v4, v19, v4, s74
	ds_write_b16_d16_hi v20, v4 offset:2432
	v_bfe_u32 v4, v28, 16, 1
	v_add3_u32 v4, v28, v4, s74
	ds_write_b16_d16_hi v20, v4 offset:2496
	v_bfe_u32 v4, v29, 16, 1
	v_add3_u32 v4, v29, v4, s74
	ds_write_b16_d16_hi v20, v4 offset:3072
	v_bfe_u32 v4, v30, 16, 1
	v_add3_u32 v4, v30, v4, s74
	ds_write_b16_d16_hi v20, v4 offset:3136
	v_bfe_u32 v4, v31, 16, 1
	v_add3_u32 v4, v31, v4, s74
	ds_write_b16_d16_hi v20, v4 offset:3200
	v_bfe_u32 v4, v32, 16, 1
	v_add3_u32 v4, v32, v4, s74
	ds_write_b16_d16_hi v20, v4 offset:3264
	v_bfe_u32 v4, v33, 16, 1
	v_add3_u32 v4, v33, v4, s74
	ds_write_b16_d16_hi v20, v4 offset:3328
	v_bfe_u32 v4, v36, 16, 1
	v_add3_u32 v4, v36, v4, s74
	ds_write_b16_d16_hi v20, v4 offset:3392
	v_bfe_u32 v4, v2, 16, 1
	s_waitcnt vmcnt(0)
	v_add_f32_e32 v3, v35, v3
	v_add3_u32 v2, v2, v4, s74
	ds_write_b16_d16_hi v20, v2 offset:3456
	v_bfe_u32 v2, v3, 16, 1
	v_add3_u32 v2, v3, v2, s74
	ds_write_b16_d16_hi v20, v2 offset:3520
	v_lshlrev_b32_e32 v2, 1, v158
	v_and_b32_e32 v130, 0x70, v2
	s_waitcnt lgkmcnt(0)
	v_lshrrev_b32_e32 v12, 3, v137
	v_add_u32_e32 v13, s76, v130
	v_lshl_add_u32 v2, v12, 7, v13
	ds_read_b128 v[2:5], v2
	v_or_b32_e32 v8, s0, v12
	v_mov_b32_e32 v9, s1
	v_lshl_add_u64 v[6:7], s[2:3], 0, v[130:131]
	v_lshlrev_b64 v[10:11], 12, v[8:9]
	v_lshl_add_u64 v[10:11], v[6:7], 0, v[10:11]
	v_or_b32_e32 v8, 8, v12
	s_waitcnt lgkmcnt(0)
	global_store_dwordx4 v[10:11], v[2:5], off
	s_nop 1
	v_lshl_add_u32 v2, v8, 7, v13
	ds_read_b128 v[2:5], v2
	v_or_b32_e32 v8, s0, v8
	v_lshlrev_b64 v[10:11], 12, v[8:9]
	v_lshl_add_u64 v[10:11], v[6:7], 0, v[10:11]
	v_or_b32_e32 v8, 16, v12
	s_waitcnt lgkmcnt(0)
	global_store_dwordx4 v[10:11], v[2:5], off
	s_nop 1
	v_lshl_add_u32 v2, v8, 7, v13
	ds_read_b128 v[2:5], v2
	v_or_b32_e32 v8, s0, v8
	v_lshlrev_b64 v[10:11], 12, v[8:9]
	v_lshl_add_u64 v[10:11], v[6:7], 0, v[10:11]
	v_or_b32_e32 v8, 24, v12
	s_waitcnt lgkmcnt(0)
	global_store_dwordx4 v[10:11], v[2:5], off
	s_nop 1
	v_lshl_add_u32 v2, v8, 7, v13
	ds_read_b128 v[2:5], v2
	v_or_b32_e32 v8, s0, v8
	v_lshlrev_b64 v[8:9], 12, v[8:9]
	v_lshl_add_u64 v[6:7], v[6:7], 0, v[8:9]
	s_waitcnt lgkmcnt(0)
	global_store_dwordx4 v[6:7], v[2:5], off
	s_waitcnt lgkmcnt(0)
	s_barrier
	s_setprio 0
	v_readlane_b32 s42, v249, 26
	v_readlane_b32 s50, v249, 30
	s_cmp_gt_i32 s60, 7
	v_readlane_b32 s43, v249, 27
	v_readlane_b32 s51, v249, 31
	s_cbranch_scc1 .LBB0_2336
	s_mul_i32 s0, s60, 48
	v_readlane_b32 s1, v248, 47
	s_add_i32 s6, s1, s0
	v_readlane_b32 s1, v248, 48
	s_add_i32 s0, s6, 48
	s_cmp_lg_u32 s60, 0
	v_mov_b32_e32 v2, s1
	v_min3_i32 v2, s0, v2, v165
	s_nop 0
	v_readfirstlane_b32 s26, v2
	s_nop 0
	s_nop 0
	s_nop 0
	s_nop 0
	s_nop 0
	s_nop 0
	s_nop 0
	s_nop 0
	s_nop 0
	s_nop 0
	s_nop 0
	s_nop 0
	s_nop 0
	s_barrier
	s_cbranch_scc1 .LBB0_2595
	v_mov_b32_e32 v109, v0
	v_readlane_b32 s0, v248, 56
	v_lshlrev_b32_e32 v2, 2, v109
	v_ashrrev_i32_e32 v3, 31, v2
	v_readlane_b32 s1, v248, 57
	s_barrier
	s_nop 0
	v_lshl_add_u64 v[2:3], v[2:3], 2, s[0:1]
	global_load_dwordx4 v[32:35], v[2:3], off
	v_add_co_u32_e32 v4, vcc, 0x2000, v2
	s_movk_i32 s0, 0x4000
	s_nop 0
	v_addc_co_u32_e32 v5, vcc, 0, v3, vcc
	global_load_dwordx4 v[26:29], v[4:5], off
	v_add_co_u32_e32 v4, vcc, s0, v2
	v_lshl_add_u32 v30, v109, 4, 0
	s_nop 0
	v_addc_co_u32_e32 v5, vcc, 0, v3, vcc
	global_load_dwordx4 v[22:25], v[4:5], off
	v_add_co_u32_e32 v4, vcc, 0x6000, v2
	v_readlane_b32 s0, v248, 49
	s_nop 0
	v_addc_co_u32_e32 v5, vcc, 0, v3, vcc
	global_load_dwordx4 v[18:21], v[4:5], off
	v_add_co_u32_e32 v4, vcc, 0x8000, v2
	v_readlane_b32 s1, v248, 50
	s_nop 0
	v_addc_co_u32_e32 v5, vcc, 0, v3, vcc
	global_load_dwordx4 v[14:17], v[4:5], off
	v_add_co_u32_e32 v4, vcc, 0xa000, v2
	v_readlane_b32 s2, v248, 58
	s_nop 0
	v_addc_co_u32_e32 v5, vcc, 0, v3, vcc
	global_load_dwordx4 v[10:13], v[4:5], off
	v_add_co_u32_e32 v4, vcc, 0xc000, v2
	v_readlane_b32 s3, v248, 59
	s_nop 0
	v_addc_co_u32_e32 v5, vcc, 0, v3, vcc
	global_load_dwordx4 v[6:9], v[4:5], off
	v_add_co_u32_e32 v2, vcc, 0xe000, v2
	s_waitcnt vmcnt(6)
	v_mul_f32_e32 v31, 0xbfb8aa3b, v32
	v_exp_f32_e32 v31, v31
	v_addc_co_u32_e32 v3, vcc, 0, v3, vcc
	global_load_dwordx4 v[2:5], v[2:3], off
	v_add_f32_e32 v31, 1.0, v31
	v_rcp_f32_e32 v36, v31
	v_mul_f32_e32 v31, 0xbfb8aa3b, v33
	v_exp_f32_e32 v31, v31
	s_andn2_b64 vcc, exec, s[0:1]
	v_add_f32_e32 v31, 1.0, v31
	v_rcp_f32_e32 v37, v31
	v_mul_f32_e32 v31, 0xbfb8aa3b, v34
	v_exp_f32_e32 v31, v31
	v_pk_mul_f32 v[32:33], v[32:33], v[36:37]
	v_add_f32_e32 v31, 1.0, v31
	v_rcp_f32_e32 v38, v31
	v_mul_f32_e32 v31, 0xbfb8aa3b, v35
	v_exp_f32_e32 v31, v31
	s_nop 0
	v_add_f32_e32 v31, 1.0, v31
	v_rcp_f32_e32 v39, v31
	s_waitcnt vmcnt(6)
	v_mul_f32_e32 v31, 0xbfb8aa3b, v26
	v_exp_f32_e32 v31, v31
	v_pk_mul_f32 v[34:35], v[34:35], v[38:39]
	ds_write_b128 v30, v[32:35]
	v_add_f32_e32 v31, 1.0, v31
	v_rcp_f32_e32 v32, v31
	v_mul_f32_e32 v31, 0xbfb8aa3b, v27
	v_exp_f32_e32 v31, v31
	s_nop 0
	v_add_f32_e32 v31, 1.0, v31
	v_rcp_f32_e32 v33, v31
	v_mul_f32_e32 v31, 0xbfb8aa3b, v28
	v_exp_f32_e32 v31, v31
	v_pk_mul_f32 v[26:27], v[26:27], v[32:33]
	v_add_f32_e32 v31, 1.0, v31
	v_rcp_f32_e32 v34, v31
	v_mul_f32_e32 v31, 0xbfb8aa3b, v29
	v_exp_f32_e32 v31, v31
	s_nop 0
	v_add_f32_e32 v31, 1.0, v31
	v_rcp_f32_e32 v35, v31
	s_nop 0
	v_pk_mul_f32 v[28:29], v[28:29], v[34:35]
	ds_write_b128 v30, v[26:29] offset:8192
	s_waitcnt vmcnt(5)
	v_mul_f32_e32 v26, 0xbfb8aa3b, v22
	v_mul_f32_e32 v27, 0xbfb8aa3b, v23
	v_mul_f32_e32 v28, 0xbfb8aa3b, v24
	v_mul_f32_e32 v29, 0xbfb8aa3b, v25
	v_exp_f32_e32 v26, v26
	v_exp_f32_e32 v27, v27
	v_exp_f32_e32 v28, v28
	v_exp_f32_e32 v29, v29
	v_add_f32_e32 v26, 1.0, v26
	v_add_f32_e32 v27, 1.0, v27
	v_add_f32_e32 v28, 1.0, v28
	v_add_f32_e32 v29, 1.0, v29
	v_rcp_f32_e32 v26, v26
	v_rcp_f32_e32 v27, v27
	v_rcp_f32_e32 v28, v28
	v_rcp_f32_e32 v29, v29
	v_pk_mul_f32 v[22:23], v[22:23], v[26:27]
	v_pk_mul_f32 v[24:25], v[24:25], v[28:29]
	ds_write_b128 v30, v[22:25] offset:16384
	s_waitcnt vmcnt(4)
	v_mul_f32_e32 v22, 0xbfb8aa3b, v18
	v_mul_f32_e32 v23, 0xbfb8aa3b, v19
	v_mul_f32_e32 v24, 0xbfb8aa3b, v20
	v_mul_f32_e32 v25, 0xbfb8aa3b, v21
	v_exp_f32_e32 v22, v22
	v_exp_f32_e32 v23, v23
	v_exp_f32_e32 v24, v24
	v_exp_f32_e32 v25, v25
	v_add_f32_e32 v22, 1.0, v22
	v_add_f32_e32 v23, 1.0, v23
	v_add_f32_e32 v24, 1.0, v24
	v_add_f32_e32 v25, 1.0, v25
	v_rcp_f32_e32 v22, v22
	v_rcp_f32_e32 v23, v23
	v_rcp_f32_e32 v24, v24
	v_rcp_f32_e32 v25, v25
	v_pk_mul_f32 v[18:19], v[18:19], v[22:23]
	v_pk_mul_f32 v[20:21], v[20:21], v[24:25]
	ds_write_b128 v30, v[18:21] offset:24576
	s_waitcnt vmcnt(3)
	v_mul_f32_e32 v18, 0xbfb8aa3b, v14
	v_mul_f32_e32 v19, 0xbfb8aa3b, v15
	v_mul_f32_e32 v20, 0xbfb8aa3b, v16
	v_mul_f32_e32 v21, 0xbfb8aa3b, v17
	v_exp_f32_e32 v18, v18
	v_exp_f32_e32 v19, v19
	v_exp_f32_e32 v20, v20
	v_exp_f32_e32 v21, v21
	v_add_f32_e32 v18, 1.0, v18
	v_add_f32_e32 v19, 1.0, v19
	v_add_f32_e32 v20, 1.0, v20
	v_add_f32_e32 v21, 1.0, v21
	v_rcp_f32_e32 v18, v18
	v_rcp_f32_e32 v19, v19
	v_rcp_f32_e32 v20, v20
	v_rcp_f32_e32 v21, v21
	v_pk_mul_f32 v[14:15], v[14:15], v[18:19]
	v_pk_mul_f32 v[16:17], v[16:17], v[20:21]
	ds_write_b128 v30, v[14:17] offset:32768
	s_waitcnt vmcnt(2)
	v_mul_f32_e32 v14, 0xbfb8aa3b, v10
	v_mul_f32_e32 v15, 0xbfb8aa3b, v11
	v_mul_f32_e32 v16, 0xbfb8aa3b, v12
	v_mul_f32_e32 v17, 0xbfb8aa3b, v13
	v_exp_f32_e32 v14, v14
	v_exp_f32_e32 v15, v15
	v_exp_f32_e32 v16, v16
	v_exp_f32_e32 v17, v17
	v_add_f32_e32 v14, 1.0, v14
	v_add_f32_e32 v15, 1.0, v15
	v_add_f32_e32 v16, 1.0, v16
	v_add_f32_e32 v17, 1.0, v17
	v_rcp_f32_e32 v14, v14
	v_rcp_f32_e32 v15, v15
	v_rcp_f32_e32 v16, v16
	v_rcp_f32_e32 v17, v17
	v_pk_mul_f32 v[10:11], v[10:11], v[14:15]
	v_pk_mul_f32 v[12:13], v[12:13], v[16:17]
	ds_write_b128 v30, v[10:13] offset:40960
	s_waitcnt vmcnt(1)
	v_mul_f32_e32 v10, 0xbfb8aa3b, v6
	v_mul_f32_e32 v11, 0xbfb8aa3b, v7
	v_mul_f32_e32 v12, 0xbfb8aa3b, v8
	v_mul_f32_e32 v13, 0xbfb8aa3b, v9
	v_exp_f32_e32 v10, v10
	v_exp_f32_e32 v11, v11
	v_exp_f32_e32 v12, v12
	v_exp_f32_e32 v13, v13
	v_add_f32_e32 v10, 1.0, v10
	v_add_f32_e32 v11, 1.0, v11
	v_add_f32_e32 v12, 1.0, v12
	v_add_f32_e32 v13, 1.0, v13
	v_rcp_f32_e32 v10, v10
	v_rcp_f32_e32 v11, v11
	v_rcp_f32_e32 v12, v12
	v_rcp_f32_e32 v13, v13
	v_pk_mul_f32 v[6:7], v[6:7], v[10:11]
	v_pk_mul_f32 v[8:9], v[8:9], v[12:13]
	ds_write_b128 v30, v[6:9] offset:49152
	s_waitcnt vmcnt(0)
	v_mul_f32_e32 v6, 0xbfb8aa3b, v2
	v_mul_f32_e32 v7, 0xbfb8aa3b, v3
	v_mul_f32_e32 v8, 0xbfb8aa3b, v4
	v_mul_f32_e32 v9, 0xbfb8aa3b, v5
	v_exp_f32_e32 v6, v6
	v_exp_f32_e32 v7, v7
	v_exp_f32_e32 v8, v8
	v_exp_f32_e32 v9, v9
	v_add_f32_e32 v6, 1.0, v6
	v_add_f32_e32 v7, 1.0, v7
	v_add_f32_e32 v8, 1.0, v8
	v_add_f32_e32 v9, 1.0, v9
	v_rcp_f32_e32 v6, v6
	v_rcp_f32_e32 v7, v7
	v_rcp_f32_e32 v8, v8
	v_rcp_f32_e32 v9, v9
	v_pk_mul_f32 v[2:3], v[2:3], v[6:7]
	v_pk_mul_f32 v[4:5], v[4:5], v[8:9]
	ds_write_b128 v30, v[2:5] offset:57344
	s_waitcnt lgkmcnt(0)
	s_barrier
	s_cbranch_vccnz .LBB0_2595
	s_movk_i32 s0, 0x1f8
	v_cmp_gt_i32_e32 vcc, s0, v109
	s_mov_b32 s0, 0x2aaaaaab
	v_mul_hi_i32 v111, v109, s0
	v_lshrrev_b32_e32 v113, 31, v111
	s_and_saveexec_b64 s[0:1], vcc
	s_cbranch_execz .LBB0_2592
	v_ashrrev_i32_e32 v2, 1, v111
	v_add_u32_e32 v115, v2, v113
	v_mul_lo_u32 v2, v115, 12
	v_sub_u32_e32 v2, v109, v2
	v_lshlrev_b32_e32 v2, 2, v2
	v_readlane_b32 s2, v248, 60
	v_ashrrev_i32_e32 v3, 31, v2
	v_readlane_b32 s3, v248, 61
	s_mov_b32 s4, 0xc000
	v_add_u32_e32 v117, 42, v115
	v_lshl_add_u64 v[62:63], v[2:3], 2, s[2:3]
	v_add_u32_e32 v119, 0x54, v115
	v_add_u32_e32 v121, 0x7e, v115
	v_add_u32_e32 v123, 0xa8, v115
	v_add_u32_e32 v125, 0xd2, v115
	v_add_u32_e32 v127, 0xfc, v115
	v_mad_i64_i32 v[2:3], s[2:3], v115, s4, v[62:63]
	v_mad_i64_i32 v[6:7], s[2:3], v117, s4, v[62:63]
	v_mad_i64_i32 v[10:11], s[2:3], v119, s4, v[62:63]
	v_mad_i64_i32 v[14:15], s[2:3], v121, s4, v[62:63]
	v_mad_i64_i32 v[18:19], s[2:3], v123, s4, v[62:63]
	v_mad_i64_i32 v[22:23], s[2:3], v125, s4, v[62:63]
	v_mad_i64_i32 v[26:27], s[2:3], v127, s4, v[62:63]
	global_load_dwordx4 v[2:5], v[2:3], off nt
	v_mov_b32_e32 v30, 0
	global_load_dwordx4 v[6:9], v[6:7], off nt
	s_mov_b32 s2, 0
	global_load_dwordx4 v[10:13], v[10:11], off nt
	v_mov_b32_e32 v31, v30
	global_load_dwordx4 v[14:17], v[14:15], off nt
	v_mov_b32_e32 v32, v30
	global_load_dwordx4 v[18:21], v[18:19], off nt
	v_mov_b32_e32 v33, v30
	global_load_dwordx4 v[22:25], v[22:23], off nt
	v_mov_b32_e32 v54, v30
	global_load_dwordx4 v[26:29], v[26:27], off nt
	v_mov_b32_e32 v55, v30
	v_mov_b32_e32 v56, v30
	v_mov_b32_e32 v57, v30
	v_mov_b32_e32 v50, v30
	v_mov_b32_e32 v51, v30
	v_mov_b32_e32 v52, v30
	v_mov_b32_e32 v53, v30
	v_mov_b32_e32 v46, v30
	v_mov_b32_e32 v47, v30
	v_mov_b32_e32 v48, v30
	v_mov_b32_e32 v49, v30
	v_mov_b32_e32 v42, v30
	v_mov_b32_e32 v43, v30
	v_mov_b32_e32 v44, v30
	v_mov_b32_e32 v45, v30
	v_mov_b32_e32 v38, v30
	v_mov_b32_e32 v39, v30
	v_mov_b32_e32 v40, v30
	v_mov_b32_e32 v41, v30
	v_mov_b32_e32 v34, v30
	v_mov_b32_e32 v35, v30
	v_mov_b32_e32 v36, v30
	v_mov_b32_e32 v37, v30
	v_mov_b32_e32 v58, v30
	v_mov_b32_e32 v59, v30
	v_mov_b32_e32 v60, v30
	v_mov_b32_e32 v61, v30
	s_waitcnt vmcnt(6)
	v_mov_b32_e32 v64, v2
	v_mov_b32_e32 v65, v3
	v_mov_b32_e32 v82, v4
	v_mov_b32_e32 v83, v5
	s_waitcnt vmcnt(5)
	v_mov_b32_e32 v84, v6
	v_mov_b32_e32 v85, v7
	v_mov_b32_e32 v86, v8
	v_mov_b32_e32 v87, v9
	s_waitcnt vmcnt(4)
	v_mov_b32_e32 v88, v10
	v_mov_b32_e32 v89, v11
	v_mov_b32_e32 v90, v12
	v_mov_b32_e32 v91, v13
	s_waitcnt vmcnt(3)
	v_mov_b32_e32 v92, v14
	v_mov_b32_e32 v93, v15
	v_mov_b32_e32 v94, v16
	v_mov_b32_e32 v95, v17
	s_waitcnt vmcnt(2)
	v_mov_b32_e32 v96, v18
	v_mov_b32_e32 v97, v19
	v_mov_b32_e32 v98, v20
	v_mov_b32_e32 v99, v21
	s_waitcnt vmcnt(1)
	v_mov_b32_e32 v100, v22
	v_mov_b32_e32 v101, v23
	v_mov_b32_e32 v102, v24
	v_mov_b32_e32 v103, v25
	s_waitcnt vmcnt(0)
	v_mov_b32_e32 v104, v26
	v_mov_b32_e32 v105, v27
	v_mov_b32_e32 v106, v28
	v_mov_b32_e32 v107, v29
	s_branch .LBB0_2477

.LBB0_2595:
	v_readlane_b32 s7, v249, 16
	s_mov_b32 s27, s26
	s_nop 0
	s_add_i32 s25, s6, s7
	s_lshr_b32 s12, s32, 10
	s_lshl_b32 s12, s12, 3
	s_add_i32 s25, s25, s12
	s_cmp_ge_i32 s25, s27
	s_cbranch_scc1 .LBB0_2335
	v_and_b32_e32 v36, 63, v0
	v_lshrrev_b32_e32 v37, 3, v36
	v_and_b32_e32 v38, 7, v36
	v_lshlrev_b32_e32 v38, 4, v38
	v_lshl_add_u32 v82, v37, 11, v38
	v_lshl_add_u32 v83, v37, 13, v38
	v_and_b32_e32 v37, 3, v36
	v_lshrrev_b32_e32 v38, 2, v36
	v_mul_u32_u24_e32 v84, 0x820, v37
	v_lshl_add_u32 v84, v38, 2, v84
	v_lshlrev_b32_e32 v85, 4, v37
	v_lshl_add_u32 v86, v38, 11, v85
	v_lshl_add_u32 v87, v38, 9, v85
	v_mov_b32_e32 v100, 0x42800000
	v_mov_b32_e32 v101, 0x42800000
	v_readlane_b32 s8, v249, 1
	v_readlane_b32 s9, v249, 2
	s_lshl_b32 s72, s7, 1
	s_mul_i32 s72, s72, 8320
	s_add_i32 s86, s72, 8320
	s_cmp_eq_u32 s7, 7
	s_cselect_b32 s86, 0x21200, s86
	s_load_dwordx2 s[10:11], s[8:9], 0xe0
	s_mov_b32 s32, 0
	s_waitcnt lgkmcnt(0)
	s_sub_u32 s7, s25, 0x3e90
	s_lshr_b32 vcc_lo, s7, 15
	s_and_b32 s7, s7, 0x7fff
	s_lshl_b32 vcc_hi, vcc_lo, 3
	s_addk_i32 vcc_hi, 0xa8
	s_load_dwordx2 s[70:71], s[8:9], vcc_hi
	s_lshr_b32 vcc_hi, s7, 9
	s_and_b32 s7, s7, 0x1ff
	s_cmp_eq_u32 vcc_lo, 2
	s_cbranch_scc1 .Lcvdb_pdn
	s_lshr_b32 s13, s7, 4
	s_and_b32 s7, s7, 15
	s_lshl_b32 s100, vcc_hi, 21
	s_lshl_b32 s101, vcc_hi, 22
	s_lshl_b32 vcc_hi, s13, 6
	s_add_u32 s100, s100, vcc_hi
	s_lshl_b32 vcc_hi, s13, 17
	s_add_u32 s101, s101, vcc_hi
	s_lshl_b32 vcc_hi, s7, 7
	s_add_u32 s101, s101, vcc_hi
	s_lshr_b32 vcc_hi, s7, 2
	s_lshl_b32 vcc_hi, vcc_hi, 19
	s_add_u32 s100, s100, vcc_hi
	s_and_b32 vcc_hi, s7, 3
	s_lshl_b32 vcc_hi, vcc_hi, 16
	s_add_u32 s100, s100, vcc_hi
	s_lshl_b32 vcc_hi, vcc_lo, 18
	s_add_u32 s100, s100, vcc_hi
	s_add_u32 s100, s100, 0x1b000000
	s_mov_b32 s61, 0x4000
	s_mov_b32 s99, 0
	s_branch .Lcvdb_pdd

.LBB0_2985:
	v_readlane_b32 s7, v249, 16
	s_mov_b32 s27, s23
	s_nop 0
	s_add_i32 s25, s58, s7
	s_cmp_ge_i32 s25, s27
	s_cbranch_scc1 .LBB0_2858
	v_and_b32_e32 v36, 63, v0
	v_lshrrev_b32_e32 v37, 3, v36
	v_and_b32_e32 v38, 7, v36
	v_lshlrev_b32_e32 v38, 4, v38
	v_lshl_add_u32 v82, v37, 11, v38
	v_lshl_add_u32 v83, v37, 13, v38
	v_and_b32_e32 v37, 3, v36
	v_lshrrev_b32_e32 v38, 2, v36
	v_mul_u32_u24_e32 v84, 0x820, v37
	v_lshl_add_u32 v84, v38, 2, v84
	v_lshlrev_b32_e32 v85, 4, v37
	v_lshl_add_u32 v86, v38, 11, v85
	v_lshl_add_u32 v87, v38, 9, v85
	v_mov_b32_e32 v100, 0x42800000
	v_mov_b32_e32 v101, 0x42800000
	v_readlane_b32 s8, v249, 1
	v_readlane_b32 s9, v249, 2
	s_lshl_b32 s72, s7, 1
	s_mul_i32 s72, s72, 8320
	s_add_i32 s86, s72, 8320
	s_cmp_eq_u32 s7, 7
	s_cselect_b32 s86, 0x21200, s86
	s_load_dwordx2 s[10:11], s[8:9], 0xe0
	s_mov_b32 s32, 0
	s_waitcnt lgkmcnt(0)
	s_sub_u32 s7, s25, 0x3e90
	s_lshr_b32 vcc_lo, s7, 15
	s_and_b32 s7, s7, 0x7fff
	s_lshl_b32 vcc_hi, vcc_lo, 3
	s_addk_i32 vcc_hi, 0xa8
	s_load_dwordx2 s[70:71], s[8:9], vcc_hi
	s_lshr_b32 vcc_hi, s7, 9
	s_and_b32 s7, s7, 0x1ff
	s_cmp_eq_u32 vcc_lo, 2
	s_cbranch_scc1 .Lcvdc_pdn
	s_lshr_b32 s13, s7, 4
	s_and_b32 s7, s7, 15
	s_lshl_b32 s100, vcc_hi, 21
	s_lshl_b32 s101, vcc_hi, 22
	s_lshl_b32 vcc_hi, s13, 6
	s_add_u32 s100, s100, vcc_hi
	s_lshl_b32 vcc_hi, s13, 17
	s_add_u32 s101, s101, vcc_hi
	s_lshl_b32 vcc_hi, s7, 7
	s_add_u32 s101, s101, vcc_hi
	s_lshr_b32 vcc_hi, s7, 2
	s_lshl_b32 vcc_hi, vcc_hi, 19
	s_add_u32 s100, s100, vcc_hi
	s_and_b32 vcc_hi, s7, 3
	s_lshl_b32 vcc_hi, vcc_hi, 16
	s_add_u32 s100, s100, vcc_hi
	s_lshl_b32 vcc_hi, vcc_lo, 18
	s_add_u32 s100, s100, vcc_hi
	s_add_u32 s100, s100, 0x1b000000
	s_mov_b32 s61, 0x4000
	s_mov_b32 s99, 0
	s_branch .Lcvdc_pdd
